# prep: code/kernarg touch loads issued first thing (global loads, before the kernarg wait) so prep's own later code lines are also warm; 72 VGPRs; stream as v23
# speedup vs baseline: 1.0174x; 1.0174x over previous
_Z11prep_kernelPKfS0_S0_S0_Pf:
	s_load_dwordx8 s[4:11], s[0:1], 0x0
	s_load_dwordx2 s[12:13], s[0:1], 0x20
	s_cmpk_eq_i32 s2, 0x100
	s_cbranch_scc1 .Lprep_exit
	s_getpc_b64 s[22:23]
	s_and_b32 s22, s22, 0xffffff00
	v_lshlrev_b32_e32 v25, 4, v0
	v_subrev_u32_e32 v30, 0x280, v0
	s_movk_i32 s24, 0x240
	v_cmp_gt_u32_e32 vcc, s24, v0
	s_and_saveexec_b64 s[20:21], vcc
	s_cbranch_execz .Lprep_pf1
	global_load_dwordx4 v[26:29], v25, s[22:23]

.Lprep_pf2:
	s_mov_b64 exec, s[20:21]
	s_and_b32 s14, s2, 63
	s_lshr_b32 s15, s2, 6
	v_and_b32_e32 v1, 7, v0
	v_and_b32_e32 v2, 0x3f8, v0
	v_lshlrev_b32_e32 v3, 10, v2
	v_lshl_or_b32 v3, v1, 4, v3
	s_lshl_b32 s16, s15, 21
	s_lshl_b32 s17, s14, 7
	s_add_i32 s16, s16, s17
	v_add_u32_e32 v3, s16, v3
	v_add_u32_e32 v4, 0x100000, v3
	v_lshrrev_b32_e32 v5, 1, v2
	s_lshl_b32 s18, s15, 10
	v_add_u32_e32 v5, s18, v5
	v_and_b32_e32 v19, 63, v0
	v_lshrrev_b32_e32 v20, 6, v0
	s_waitcnt lgkmcnt(0)
	global_load_dwordx4 v[8:11], v3, s[4:5] nt
	global_load_dwordx4 v[12:15], v4, s[4:5] nt
	global_load_dword v6, v5, s[6:7]
	global_load_dword v16, v5, s[6:7] offset:512
	s_cmp_lt_u32 s14, 32
	s_cbranch_scc0 .Lprep_ld_done
	v_cmp_gt_u32_e32 vcc, 0x200, v0
	s_and_saveexec_b64 s[20:21], vcc
	s_cbranch_execz .Lprep_hb_skip
	v_lshrrev_b32_e32 v17, 5, v0
	v_and_b32_e32 v18, 31, v0
	v_lshlrev_b32_e32 v17, 12, v17
	v_lshl_or_b32 v17, v18, 2, v17
	v_add_u32_e32 v17, s17, v17
	global_load_dword v36, v17, s[10:11]
